# v47 + MLA loop: running-reference update (fmamk/max/sub/exp + 2 cndmask per half tile) branched out of line on the existing wave-uniform all-lanes test; common path two v_mov
# speedup vs baseline: 1.0193x; 1.0136x over previous
.LBB0_565:
	s_waitcnt lgkmcnt(4)
	v_mfma_scale_f32_32x32x64_f8f6f4 v[96:111], v[96:103], v[120:127], 0, v205, v205 op_sel_hi:[0,0,0]
	v_cndmask_b32_e64 v176, v189, v192, s[4:5]
	v_fma_f32 v80, v80, s40, -v176
	v_fma_f32 v81, v81, s40, -v176
	v_fma_f32 v84, v84, s40, -v176
	v_fma_f32 v85, v85, s40, -v176
	v_fma_f32 v88, v88, s40, -v176
	v_fma_f32 v89, v89, s40, -v176
	v_fma_f32 v92, v92, s40, -v176
	v_fma_f32 v93, v93, s40, -v176
	v_exp_f32_e32 v80, v80
	v_exp_f32_e32 v81, v81
	v_exp_f32_e32 v84, v84
	v_exp_f32_e32 v85, v85
	v_exp_f32_e32 v88, v88
	v_exp_f32_e32 v89, v89
	s_waitcnt lgkmcnt(2)
	v_mfma_scale_f32_32x32x64_f8f6f4 v[96:111], v[156:163], v[128:135], v[96:111], v205, v205 op_sel_hi:[0,0,0]
	v_exp_f32_e32 v92, v92
	v_exp_f32_e32 v93, v93
	v_fma_f32 v82, v82, s40, -v176
	v_fma_f32 v83, v83, s40, -v176
	v_fma_f32 v86, v86, s40, -v176
	v_fma_f32 v87, v87, s40, -v176
	v_fma_f32 v90, v90, s40, -v176
	v_fma_f32 v91, v91, s40, -v176
	v_fma_f32 v94, v94, s40, -v176
	v_fma_f32 v95, v95, s40, -v176
	v_exp_f32_e32 v82, v82
	v_exp_f32_e32 v83, v83
	v_exp_f32_e32 v86, v86
	v_exp_f32_e32 v87, v87
	v_exp_f32_e32 v90, v90
	s_waitcnt lgkmcnt(0)
	v_mfma_scale_f32_32x32x64_f8f6f4 v[96:111], v[148:155], v[136:143], v[96:111], v205, v205 op_sel_hi:[0,0,0]
	v_lshl_add_u32 v240, s23, 14, v211
	ds_read_b128 v[224:227], v240
	ds_read_b128 v[228:231], v240 offset:16
	ds_read_b128 v[232:235], v240 offset:2560
	ds_read_b128 v[236:239], v240 offset:2576
	v_exp_f32_e32 v91, v91
	v_exp_f32_e32 v94, v94
	v_exp_f32_e32 v95, v95
	v_cvt_pk_fp8_f32 v148, v80, v81
	v_cvt_pk_fp8_f32 v149, v84, v85
	v_cvt_pk_fp8_f32 v150, v88, v89
	v_cvt_pk_fp8_f32 v151, v92, v93
	v_cvt_pk_fp8_f32 v148, v82, v83 op_sel:[0,0,1]
	v_cvt_pk_fp8_f32 v149, v86, v87 op_sel:[0,0,1]
	v_cvt_pk_fp8_f32 v150, v90, v91 op_sel:[0,0,1]
	v_cvt_pk_fp8_f32 v151, v94, v95 op_sel:[0,0,1]
	s_nop 0
	s_waitcnt lgkmcnt(2)
	v_mfma_scale_f32_32x32x64_f8f6f4 v[48:63], v[144:151], v[224:231], v[48:63], v205, v205 op_sel_hi:[0,0,0]
	ds_read_b128 v[80:83], v240 offset:5120
	ds_read_b128 v[84:87], v240 offset:5136
	ds_read_b128 v[152:155], v240 offset:7680
	ds_read_b128 v[156:159], v240 offset:7696
	s_waitcnt lgkmcnt(4)
	v_mfma_scale_f32_32x32x64_f8f6f4 v[32:47], v[144:151], v[232:239], v[32:47], v205, v205 op_sel_hi:[0,0,0]
	v_max_f32_e32 v88, v96, v97
	v_max3_f32 v88, v88, v98, v99
	v_max3_f32 v88, v88, v100, v101
	v_max3_f32 v88, v88, v102, v103
	v_max3_f32 v88, v88, v104, v105
	v_max3_f32 v88, v88, v106, v107
	s_waitcnt lgkmcnt(2)
	v_mfma_scale_f32_32x32x64_f8f6f4 v[16:31], v[144:151], v[80:87], v[16:31], v205, v205 op_sel_hi:[0,0,0]
	v_max3_f32 v88, v88, v108, v109
	v_max3_f32 v88, v88, v110, v111
	v_mov_b32_e32 v89, v88
	s_nop 1
	v_permlane32_swap_b32_e32 v88, v89
	v_max_f32_e32 v80, v88, v89
	v_fma_f32 v81, v80, s40, -v176
	v_cmp_ge_f32_e32 vcc, s70, v81
	s_waitcnt lgkmcnt(0)
	v_mfma_scale_f32_32x32x64_f8f6f4 v[0:15], v[144:151], v[152:159], v[0:15], v205, v205 op_sel_hi:[0,0,0]
	s_cmp_eq_u64 vcc, exec
	s_cbranch_scc0 .Lmla_rare_a0
	v_mov_b32_e32 v192, v176
	v_mov_b32_e32 v88, 1.0
.Lmla_back_a0:
	s_add_i32 s21, s21, 2
	s_add_i32 s78, s78, 1
	s_add_i32 s22, s22, 64
	v_fma_f32 v178, v96, s40, -v192
	v_fma_f32 v179, v97, s40, -v192
	v_fma_f32 v176, v98, s40, -v192
	v_fma_f32 v177, v99, s40, -v192
	v_fma_f32 v162, v100, s40, -v192
	v_fma_f32 v163, v101, s40, -v192
	v_fma_f32 v160, v102, s40, -v192
	v_fma_f32 v161, v103, s40, -v192
	v_fma_f32 v158, v104, s40, -v192
	v_fma_f32 v159, v105, s40, -v192
	v_fma_f32 v156, v106, s40, -v192
	v_fma_f32 v157, v107, s40, -v192
	v_fma_f32 v154, v108, s40, -v192
	v_fma_f32 v155, v109, s40, -v192
	v_fma_f32 v152, v110, s40, -v192
	v_fma_f32 v153, v111, s40, -v192
	v_mfma_scale_f32_32x32x64_f8f6f4 v[64:79], v[144:151], v[112:119], v[64:79], v205, v205 op_sel_hi:[0,0,0]
	s_cmp_ge_u32 s21, s17
	s_barrier
	s_cbranch_scc1 .LBB0_580

.LBB0_577:
	s_cmp_eq_u64 vcc, s[4:5]
	s_cbranch_scc0 .Lmla_rare_b0
	s_mov_b64 s[4:5], -1
	v_mov_b32_e32 v191, 1.0
.Lmla_back_b0:
	v_exp_f32_e32 v97, v179
	v_exp_f32_e32 v96, v178
	v_exp_f32_e32 v100, v162
	v_exp_f32_e32 v101, v163
	v_exp_f32_e32 v104, v158
	v_exp_f32_e32 v105, v159
	v_exp_f32_e32 v108, v154
	v_exp_f32_e32 v109, v155
	v_exp_f32_e32 v98, v176
	v_exp_f32_e32 v99, v177
	v_exp_f32_e32 v102, v160
	v_exp_f32_e32 v103, v161
	v_cvt_pk_fp8_f32 v144, v96, v97
	v_cvt_pk_fp8_f32 v145, v100, v101
	s_xor_b32 s18, s24, 0x8000
	v_exp_f32_e32 v106, v156
	v_exp_f32_e32 v107, v157
	v_exp_f32_e32 v110, v152
	v_cvt_pk_fp8_f32 v146, v104, v105
	v_exp_f32_e32 v104, v153
	v_cvt_pk_fp8_f32 v147, v108, v109
	v_add_u32_e32 v105, s18, v216
	v_cvt_pk_fp8_f32 v144, v98, v99 op_sel:[0,0,1]
	v_cvt_pk_fp8_f32 v145, v102, v103 op_sel:[0,0,1]
	s_waitcnt lgkmcnt(0)
	s_barrier
	ds_read_b128 v[96:99], v105
	ds_read_b128 v[100:103], v105 offset:16
	ds_read_b128 v[156:159], v105 offset:64
	ds_read_b128 v[160:163], v105 offset:80
	v_add_u32_e32 v105, v105, v217
	ds_read_b128 v[148:151], v105 offset:128
	ds_read_b128 v[152:155], v105 offset:160
	v_cvt_pk_fp8_f32 v146, v106, v107 op_sel:[0,0,1]
	v_cvt_pk_fp8_f32 v147, v110, v104 op_sel:[0,0,1]
	v_cmp_gt_f32_e32 vcc, 1.0, v191
	s_cbranch_vccz .LBB0_565
	s_and_saveexec_b64 s[18:19], s[2:3]
	s_cbranch_execz .LBB0_564
	ds_write_b32 v209, v191 offset:128
	s_branch .LBB0_564
.Lmla_rare_a0:
	v_fmamk_f32 v80, v80, 0x3dd53b94, v202
	v_max_f32_e32 v192, v176, v80
	v_sub_f32_e32 v81, v176, v192
	v_exp_f32_e32 v88, v81
	s_branch .Lmla_back_a0
.Lmla_rare_b0:
	v_mul_f32_e32 v96, 0x3dd53b94, v96
	v_add_f32_e32 v96, 0xc0a00000, v96
	v_max_f32_e32 v189, v192, v96
	v_sub_f32_e32 v96, v192, v189
	v_exp_f32_e32 v191, v96
	s_mov_b64 s[4:5], 0
	s_branch .Lmla_back_b0

.LBB0_1875:
	s_waitcnt lgkmcnt(4)
	v_mfma_scale_f32_32x32x64_f8f6f4 v[96:111], v[96:103], v[120:127], 0, v207, v207 op_sel_hi:[0,0,0]
	v_cndmask_b32_e64 v176, v191, v194, s[4:5]
	v_fma_f32 v80, v80, s38, -v176
	v_fma_f32 v81, v81, s38, -v176
	v_fma_f32 v84, v84, s38, -v176
	v_fma_f32 v85, v85, s38, -v176
	v_fma_f32 v88, v88, s38, -v176
	v_fma_f32 v89, v89, s38, -v176
	v_fma_f32 v92, v92, s38, -v176
	v_fma_f32 v93, v93, s38, -v176
	v_exp_f32_e32 v80, v80
	v_exp_f32_e32 v81, v81
	v_exp_f32_e32 v84, v84
	v_exp_f32_e32 v85, v85
	v_exp_f32_e32 v88, v88
	v_exp_f32_e32 v89, v89
	s_waitcnt lgkmcnt(2)
	v_mfma_scale_f32_32x32x64_f8f6f4 v[96:111], v[156:163], v[128:135], v[96:111], v207, v207 op_sel_hi:[0,0,0]
	v_exp_f32_e32 v92, v92
	v_exp_f32_e32 v93, v93
	v_fma_f32 v82, v82, s38, -v176
	v_fma_f32 v83, v83, s38, -v176
	v_fma_f32 v86, v86, s38, -v176
	v_fma_f32 v87, v87, s38, -v176
	v_fma_f32 v90, v90, s38, -v176
	v_fma_f32 v91, v91, s38, -v176
	v_fma_f32 v94, v94, s38, -v176
	v_fma_f32 v95, v95, s38, -v176
	v_exp_f32_e32 v82, v82
	v_exp_f32_e32 v83, v83
	v_exp_f32_e32 v86, v86
	v_exp_f32_e32 v87, v87
	v_exp_f32_e32 v90, v90
	s_waitcnt lgkmcnt(0)
	v_mfma_scale_f32_32x32x64_f8f6f4 v[96:111], v[148:155], v[136:143], v[96:111], v207, v207 op_sel_hi:[0,0,0]
	v_lshl_add_u32 v240, s24, 14, v209
	ds_read_b128 v[224:227], v240
	ds_read_b128 v[228:231], v240 offset:16
	ds_read_b128 v[232:235], v240 offset:2560
	ds_read_b128 v[236:239], v240 offset:2576
	v_exp_f32_e32 v91, v91
	v_exp_f32_e32 v94, v94
	v_exp_f32_e32 v95, v95
	v_cvt_pk_fp8_f32 v148, v80, v81
	v_cvt_pk_fp8_f32 v149, v84, v85
	v_cvt_pk_fp8_f32 v150, v88, v89
	v_cvt_pk_fp8_f32 v151, v92, v93
	v_cvt_pk_fp8_f32 v148, v82, v83 op_sel:[0,0,1]
	v_cvt_pk_fp8_f32 v149, v86, v87 op_sel:[0,0,1]
	v_cvt_pk_fp8_f32 v150, v90, v91 op_sel:[0,0,1]
	v_cvt_pk_fp8_f32 v151, v94, v95 op_sel:[0,0,1]
	s_nop 0
	s_waitcnt lgkmcnt(2)
	v_mfma_scale_f32_32x32x64_f8f6f4 v[48:63], v[144:151], v[224:231], v[48:63], v207, v207 op_sel_hi:[0,0,0]
	ds_read_b128 v[80:83], v240 offset:5120
	ds_read_b128 v[84:87], v240 offset:5136
	ds_read_b128 v[152:155], v240 offset:7680
	ds_read_b128 v[156:159], v240 offset:7696
	s_waitcnt lgkmcnt(4)
	v_mfma_scale_f32_32x32x64_f8f6f4 v[32:47], v[144:151], v[232:239], v[32:47], v207, v207 op_sel_hi:[0,0,0]
	v_max_f32_e32 v88, v96, v97
	v_max3_f32 v88, v88, v98, v99
	v_max3_f32 v88, v88, v100, v101
	v_max3_f32 v88, v88, v102, v103
	v_max3_f32 v88, v88, v104, v105
	v_max3_f32 v88, v88, v106, v107
	s_waitcnt lgkmcnt(2)
	v_mfma_scale_f32_32x32x64_f8f6f4 v[16:31], v[144:151], v[80:87], v[16:31], v207, v207 op_sel_hi:[0,0,0]
	v_max3_f32 v88, v88, v108, v109
	v_max3_f32 v88, v88, v110, v111
	v_mov_b32_e32 v89, v88
	s_nop 1
	v_permlane32_swap_b32_e32 v88, v89
	v_max_f32_e32 v80, v88, v89
	v_fma_f32 v81, v80, s38, -v176
	v_cmp_ge_f32_e32 vcc, s68, v81
	s_waitcnt lgkmcnt(0)
	v_mfma_scale_f32_32x32x64_f8f6f4 v[0:15], v[144:151], v[152:159], v[0:15], v207, v207 op_sel_hi:[0,0,0]
	s_cmp_eq_u64 vcc, exec
	s_cbranch_scc0 .Lmla_rare_a1
	v_mov_b32_e32 v194, v176
	v_mov_b32_e32 v88, 1.0
.Lmla_back_a1:
	v_fma_f32 v178, v96, s38, -v194
	v_fma_f32 v179, v97, s38, -v194
	v_fma_f32 v176, v98, s38, -v194
	v_fma_f32 v177, v99, s38, -v194
	v_fma_f32 v162, v100, s38, -v194
	v_fma_f32 v163, v101, s38, -v194
	v_fma_f32 v160, v102, s38, -v194
	v_fma_f32 v161, v103, s38, -v194
	v_fma_f32 v158, v104, s38, -v194
	v_fma_f32 v159, v105, s38, -v194
	v_fma_f32 v156, v106, s38, -v194
	v_fma_f32 v157, v107, s38, -v194
	v_fma_f32 v154, v108, s38, -v194
	v_fma_f32 v155, v109, s38, -v194
	v_fma_f32 v152, v110, s38, -v194
	v_fma_f32 v153, v111, s38, -v194
	s_add_i32 s17, s17, 2
	s_add_i32 s76, s76, 1
	s_and_b64 vcc, exec, s[18:19]
	v_mfma_scale_f32_32x32x64_f8f6f4 v[64:79], v[144:151], v[112:119], v[64:79], v207, v207 op_sel_hi:[0,0,0]
	s_barrier
	s_cbranch_vccnz .LBB0_1889

.LBB0_1886:
	s_cmp_eq_u64 s[4:5], s[20:21]
	s_cbranch_scc0 .Lmla_rare_b1
	s_mov_b64 s[4:5], -1
	v_mov_b32_e32 v193, 1.0
.Lmla_back_b1:
	v_exp_f32_e32 v97, v179
	v_exp_f32_e32 v96, v178
	v_exp_f32_e32 v100, v162
	v_exp_f32_e32 v101, v163
	v_exp_f32_e32 v104, v158
	v_exp_f32_e32 v105, v159
	v_exp_f32_e32 v108, v154
	v_exp_f32_e32 v109, v155
	v_exp_f32_e32 v98, v176
	v_exp_f32_e32 v99, v177
	v_exp_f32_e32 v102, v160
	v_exp_f32_e32 v103, v161
	v_cvt_pk_fp8_f32 v144, v96, v97
	v_cvt_pk_fp8_f32 v145, v100, v101
	s_xor_b32 s20, s25, 0x8000
	v_exp_f32_e32 v106, v156
	v_exp_f32_e32 v107, v157
	v_exp_f32_e32 v110, v152
	v_cvt_pk_fp8_f32 v146, v104, v105
	v_exp_f32_e32 v104, v153
	v_cvt_pk_fp8_f32 v147, v108, v109
	v_add_u32_e32 v105, s20, v214
	v_cvt_pk_fp8_f32 v144, v98, v99 op_sel:[0,0,1]
	v_cvt_pk_fp8_f32 v145, v102, v103 op_sel:[0,0,1]
	s_waitcnt lgkmcnt(0)
	s_barrier
	ds_read_b128 v[96:99], v105
	ds_read_b128 v[100:103], v105 offset:16
	ds_read_b128 v[156:159], v105 offset:64
	ds_read_b128 v[160:163], v105 offset:80
	v_add_u32_e32 v105, v105, v215
	ds_read_b128 v[148:151], v105 offset:128
	ds_read_b128 v[152:155], v105 offset:160
	v_cvt_pk_fp8_f32 v146, v106, v107 op_sel:[0,0,1]
	v_cvt_pk_fp8_f32 v147, v110, v104 op_sel:[0,0,1]
	v_cmp_gt_f32_e32 vcc, 1.0, v193
	s_cbranch_vccz .LBB0_1875
	s_and_saveexec_b64 s[20:21], s[2:3]
	s_cbranch_execz .LBB0_1874
	ds_write_b32 v208, v193 offset:128
	s_branch .LBB0_1874
.Lmla_rare_a1:
	v_fmamk_f32 v80, v80, 0x3dd53b94, v204
	v_max_f32_e32 v194, v176, v80
	v_sub_f32_e32 v81, v176, v194
	v_exp_f32_e32 v88, v81
	s_branch .Lmla_back_a1
.Lmla_rare_b1:
	v_mul_f32_e32 v96, 0x3dd53b94, v96
	v_add_f32_e32 v96, 0xc0a00000, v96
	v_max_f32_e32 v191, v194, v96
	v_sub_f32_e32 v96, v194, v191
	v_exp_f32_e32 v193, v96
	s_mov_b64 s[4:5], 0
	s_branch .Lmla_back_b1
